# attn VT staging remapped: consecutive lanes load/write consecutive 16-byte pieces (coalesced loads, conflict-free ds_write_b128)
# speedup vs baseline: 1.0185x; 1.0092x over previous
_Z11attn_kernelPKfS0_PKDF16_S0_S0_S0_S2_PDF16_S3_:
	s_load_dwordx16 s[4:19], s[0:1], 0x0
	s_load_dwordx2 s[62:63], s[0:1], 0x40
	v_readfirstlane_b32 s49, v0
	s_and_b32 s22, s2, 7
	s_lshr_b32 s23, s2, 3
	s_lshl_b32 s43, s22, 1
	s_and_b32 s24, s23, 1
	s_or_b32 s33, s43, s24
	s_lshr_b32 s41, s2, 4
	s_mul_i32 s41, s41, 24
	s_lshr_b32 s51, s49, 6
	s_mul_i32 s34, s33, 0xc0
	s_mov_b32 s35, 0
	s_lshl_b32 s25, s33, 5
	s_lshl_b32 s42, s22, 5
	s_add_i32 s42, s42, s23
	s_lshl_b32 s42, s42, 10
	s_add_i32 s36, s41, 23
	s_lshr_b32 s36, s36, 4
	s_and_b32 s36, s36, 0xffffffc
	s_lshr_b32 s37, s41, 4
	s_and_b32 s37, s37, 0xffffffc
	s_movk_i32 s40, 0x200
	v_lshrrev_b32_e32 v34, 5, v0
	v_bfe_u32 v35, v0, 1, 4
	v_mov_b32_e32 v115, 0
	v_lshlrev_b32_e32 v116, 4, v0
	v_add_u32_e32 v2, s41, v34
	v_lshrrev_b32_e32 v2, 1, v2
	v_mov_b32_e32 v3, v115
	v_lshl_add_u64 v[2:3], s[34:35], 0, v[2:3]
	v_lshlrev_b64 v[2:3], 9, v[2:3]
	v_lshlrev_b32_e32 v4, 5, v35
	v_mov_b32_e32 v5, v115
	v_lshrrev_b32_e32 v8, 3, v0
	v_and_b32_e32 v8, 4, v8
	v_mov_b32_e32 v9, v115
	v_lshrrev_b32_e32 v36, 4, v0
	s_movk_i32 s26, 0xab
	v_mul_u32_u24_e32 v36, s26, v36
	v_lshrrev_b32_e32 v36, 9, v36
	v_mul_u32_u24_e32 v37, 48, v36
	v_sub_u32_e32 v37, v0, v37
	s_lshl_b32 s27, s33, 6
	v_add_u32_e32 v38, s27, v36
	v_mul_u32_u24_e32 v38, 0x300, v38
	v_lshl_add_u32 v38, v37, 4, v38
	v_mul_u32_u24_e32 v39, 0x320, v36
	v_lshl_add_u32 v39, v37, 4, v39
	v_add_u32_e32 v39, 0x8000, v39
	s_waitcnt lgkmcnt(0)
	s_add_u32 s26, s12, s25
	s_addc_u32 s27, s13, 0
	s_load_dword s52, s[26:27], s36 offset:0x0
	s_load_dword s53, s[26:27], s37 offset:0x0
	s_load_dwordx4 s[56:59], s[12:13], s25 offset:0x200
	s_load_dwordx2 s[60:61], s[12:13], s25 offset:0x210
	s_load_dwordx2 s[28:29], s[12:13], 0x400
	v_lshl_add_u64 v[2:3], s[4:5], 0, v[2:3]
	v_lshl_add_u64 v[6:7], v[2:3], 0, v[4:5]
	v_lshlrev_b32_e32 v2, 4, v35
	v_lshl_add_u64 v[10:11], v[6:7], 0, v[8:9]
	global_load_dwordx4 v[2:5], v2, s[10:11]
	s_nop 0
	global_load_dword v8, v[10:11], off offset:24
	global_load_dword v6, v[10:11], off
	global_load_dword v7, v[10:11], off offset:8
	global_load_dword v9, v[10:11], off offset:16
	s_waitcnt lgkmcnt(0)
	v_max_f32_e64 v10, s52, s52
	v_max_f32_e64 v11, s53, s53
	v_max_f32_e32 v10, v11, v10
	v_max_f32_e64 v11, s57, s57
	v_max_f32_e64 v12, s56, s56
	v_max_f32_e32 v11, v12, v11
	v_max_f32_e64 v12, s59, s59
	v_max_f32_e64 v13, s58, s58
	v_max_f32_e32 v12, v13, v12
	v_max_f32_e64 v13, s61, s61
	v_max_f32_e64 v14, s60, s60
	v_max_f32_e32 v13, v14, v13
	v_max3_f32 v11, v11, v12, v13
	s_mov_b32 s24, 0x41700000
	v_cmp_gt_f32_e32 vcc, s24, v10
	v_cmp_gt_f32_e64 s[26:27], s24, v11
	s_and_b64 s[26:27], vcc, s[26:27]
	v_cmp_lt_f32_e64 s[36:37], s29, 4.0
	s_and_b64 s[26:27], s[26:27], s[36:37]
	v_max_f32_e32 v12, v10, v10
	v_max_f32_e32 v12, 1.0, v12
	v_mul_f32_e32 v13, v12, v12
	v_mul_f32_e32 v13, v12, v13
	v_mul_f32_e32 v12, v12, v13
	v_mul_f32_e32 v12, s29, v12
	s_mov_b32 s24, 0x476a6000
	v_cmp_gt_f32_e64 s[36:37], s24, v12
	s_and_b64 s[26:27], s[26:27], s[36:37]
	s_andn2_b64 vcc, exec, s[26:27]
	s_cbranch_vccz .Lf_fast
	s_waitcnt vmcnt(0)
	s_branch .Lattn_orig

.Lf_27:
	s_or_b64 exec, exec, s[2:3]
	v_and_b32_e32 v2, 0x3f0, v116
	v_add_u32_e32 v166, 0, v2
	s_waitcnt lgkmcnt(0)
	s_barrier
	s_mov_b32 s46, s8
	s_mov_b32 s47, s9
	global_load_dwordx4 v[66:69], v38, s[46:47]
	s_add_u32 s46, s46, 0x3000
	s_addc_u32 s47, s47, 0
	global_load_dwordx4 v[70:73], v38, s[46:47]
	s_add_u32 s46, s46, 0x3000
	s_addc_u32 s47, s47, 0
	global_load_dwordx4 v[74:77], v38, s[46:47]
	s_add_u32 s46, s46, 0x3000
	s_addc_u32 s47, s47, 0
	global_load_dwordx4 v[78:81], v38, s[46:47]
	v_and_b32_e32 v167, 31, v0
	v_lshl_or_b32 v167, s51, 5, v167
	s_mul_i32 s38, s33, 0x1800
	v_add_u32_e32 v2, s38, v167
	v_lshlrev_b32_e32 v2, 5, v2
	v_bfe_u32 v3, v0, 5, 1
	v_lshl_add_u32 v2, v3, 4, v2
	s_mov_b32 s44, s16
	s_mov_b32 s45, s17
	global_load_dwordx4 v[102:105], v2, s[44:45]
	s_add_u32 s44, s44, 0x3000
	s_addc_u32 s45, s45, 0
	global_load_dwordx4 v[106:109], v2, s[44:45]
	s_add_u32 s44, s44, 0x3000
	s_addc_u32 s45, s45, 0
	global_load_dwordx4 v[110:113], v2, s[44:45]
	s_add_u32 s44, s44, 0x3000
	s_addc_u32 s45, s45, 0
	global_load_dwordx4 v[114:117], v2, s[44:45]
	s_add_u32 s44, s44, 0x3000
	s_addc_u32 s45, s45, 0
	global_load_dwordx4 v[118:121], v2, s[44:45]
	s_add_u32 s44, s44, 0x3000
	s_addc_u32 s45, s45, 0
	global_load_dwordx4 v[122:125], v2, s[44:45]
	s_add_u32 s44, s44, 0x3000
	s_addc_u32 s45, s45, 0
	global_load_dwordx4 v[126:129], v2, s[44:45]
	s_add_u32 s44, s44, 0x3000
	s_addc_u32 s45, s45, 0
	global_load_dwordx4 v[130:133], v2, s[44:45]
	s_add_u32 s44, s44, 0x3000
	s_addc_u32 s45, s45, 0
	global_load_dwordx4 v[134:137], v2, s[44:45]
	s_add_u32 s44, s44, 0x3000
	s_addc_u32 s45, s45, 0
	global_load_dwordx4 v[138:141], v2, s[44:45]
	s_add_u32 s44, s44, 0x3000
	s_addc_u32 s45, s45, 0
	global_load_dwordx4 v[142:145], v2, s[44:45]
	s_add_u32 s44, s44, 0x3000
	s_addc_u32 s45, s45, 0
	global_load_dwordx4 v[146:149], v2, s[44:45]
	s_add_u32 s44, s44, 0x3000
	s_addc_u32 s45, s45, 0
	global_load_dwordx4 v[150:153], v2, s[44:45]
	s_add_u32 s44, s44, 0x3000
	s_addc_u32 s45, s45, 0
	global_load_dwordx4 v[154:157], v2, s[44:45]
	s_add_u32 s44, s44, 0x3000
	s_addc_u32 s45, s45, 0
	global_load_dwordx4 v[158:161], v2, s[44:45]
	s_add_u32 s44, s44, 0x3000
	s_addc_u32 s45, s45, 0
	global_load_dwordx4 v[162:165], v2, s[44:45]
	v_mul_u32_u24_e32 v1, 0xc80, v3
	v_lshl_add_u32 v1, v167, 1, v1
	v_add_u32_e32 v1, 0x18000, v1
	v_mov_b32_e32 v167, v39
	v_mov_b32_e32 v90, 0
	v_mov_b32_e32 v91, 0
	v_mov_b32_e32 v92, 0
	v_mov_b32_e32 v93, 0
	v_mov_b32_e32 v94, 0
	v_mov_b32_e32 v95, 0
	v_mov_b32_e32 v96, 0
	v_mov_b32_e32 v97, 0
	v_mov_b32_e32 v98, 0
	v_mov_b32_e32 v99, 0
	v_mov_b32_e32 v100, 0
	v_mov_b32_e32 v101, 0
	ds_read_b128 v[46:49], v166 offset:2048
	ds_read_b128 v[14:17], v166 offset:0
	ds_read_b128 v[30:33], v166 offset:1024
	ds_read_b128 v[62:65], v166 offset:3072
	s_waitcnt vmcnt(14) lgkmcnt(3)
	v_mfma_f32_32x32x16_f16 v[34:49], v[46:49], v[106:109], 0
	s_waitcnt lgkmcnt(2)
	v_mfma_f32_32x32x16_f16 v[2:17], v[14:17], v[102:105], 0
	s_waitcnt lgkmcnt(1)
	v_mfma_f32_32x32x16_f16 v[18:33], v[30:33], v[102:105], 0
	s_waitcnt lgkmcnt(0)
	v_mfma_f32_32x32x16_f16 v[50:65], v[62:65], v[106:109], 0
	ds_write_b128 v167, v[66:69]
	ds_write_b128 v167, v[70:73] offset:12800
	ds_write_b128 v167, v[74:77] offset:25600
	ds_write_b128 v167, v[78:81] offset:38400
	s_lshl_b32 s22, s42, 2
	s_cmpk_lt_u32 s49, 0x100
	s_cselect_b32 s20, s14, s10
	s_cselect_b32 s21, s15, s11
	s_cselect_b32 s22, s22, 0
	s_cselect_b32 s23, 0xff, 15
	v_and_b32_e32 v82, s23, v0
	v_lshlrev_b32_e32 v82, 4, v82
	v_add_u32_e32 v82, s22, v82
	global_load_dwordx4 v[102:105], v82, s[20:21]
	s_nop 7
	ds_read_b128 v[46:49], v166 offset:6144
	ds_read_b128 v[14:17], v166 offset:4096
	ds_read_b128 v[30:33], v166 offset:5120
	ds_read_b128 v[62:65], v166 offset:7168
	v_pk_mul_f32 v[66:67], v[34:35], v[18:19]
	v_pk_mul_f32 v[68:69], v[36:37], v[20:21]
	v_pk_mul_f32 v[70:71], v[38:39], v[22:23]
	v_pk_mul_f32 v[72:73], v[40:41], v[24:25]
	v_pk_mul_f32 v[74:75], v[42:43], v[26:27]
	v_pk_mul_f32 v[76:77], v[44:45], v[28:29]
	s_waitcnt vmcnt(13) lgkmcnt(3)
	v_mfma_f32_32x32x16_f16 v[34:49], v[46:49], v[114:117], 0
	v_pk_fma_f32 v[66:67], v[2:3], v[50:51], v[66:67]
	v_pk_fma_f32 v[68:69], v[4:5], v[52:53], v[68:69]
	v_pk_fma_f32 v[70:71], v[6:7], v[54:55], v[70:71]
	v_pk_fma_f32 v[72:73], v[8:9], v[56:57], v[72:73]
	v_pk_fma_f32 v[74:75], v[10:11], v[58:59], v[74:75]
	v_pk_fma_f32 v[76:77], v[12:13], v[60:61], v[76:77]
	s_waitcnt lgkmcnt(2)
	v_mfma_f32_32x32x16_f16 v[2:17], v[14:17], v[110:113], 0
	v_pk_mul_f32 v[78:79], v[18:19], v[50:51]
	v_pk_mul_f32 v[80:81], v[20:21], v[52:53]
	v_pk_mul_f32 v[82:83], v[22:23], v[54:55]
	v_pk_mul_f32 v[84:85], v[24:25], v[56:57]
	v_pk_mul_f32 v[86:87], v[26:27], v[58:59]
	v_pk_mul_f32 v[88:89], v[28:29], v[60:61]
	s_waitcnt lgkmcnt(1)
	v_mfma_f32_32x32x16_f16 v[18:33], v[30:33], v[110:113], 0
	s_waitcnt lgkmcnt(0)
	v_mfma_f32_32x32x16_f16 v[50:65], v[62:65], v[114:117], 0
	v_rcp_f32_e32 v78, v78
	v_rcp_f32_e32 v79, v79
	v_rcp_f32_e32 v80, v80
	v_rcp_f32_e32 v81, v81
	v_rcp_f32_e32 v82, v82
	v_rcp_f32_e32 v83, v83
	v_rcp_f32_e32 v84, v84
	v_rcp_f32_e32 v85, v85
	v_rcp_f32_e32 v86, v86
	v_rcp_f32_e32 v87, v87
	v_rcp_f32_e32 v88, v88
	v_rcp_f32_e32 v89, v89
	v_pk_fma_f32 v[90:91], v[66:67], v[78:79], v[90:91]
	v_pk_fma_f32 v[92:93], v[68:69], v[80:81], v[92:93]
	v_pk_fma_f32 v[94:95], v[70:71], v[82:83], v[94:95]
	v_pk_fma_f32 v[96:97], v[72:73], v[84:85], v[96:97]
	v_pk_fma_f32 v[98:99], v[74:75], v[86:87], v[98:99]
	v_pk_fma_f32 v[100:101], v[76:77], v[88:89], v[100:101]
	ds_read_b128 v[46:49], v166 offset:10240
	ds_read_b128 v[14:17], v166 offset:8192
	ds_read_b128 v[30:33], v166 offset:9216
	ds_read_b128 v[62:65], v166 offset:11264
	v_pk_mul_f32 v[66:67], v[34:35], v[18:19]
	v_pk_mul_f32 v[68:69], v[36:37], v[20:21]
	v_pk_mul_f32 v[70:71], v[38:39], v[22:23]
	v_pk_mul_f32 v[72:73], v[40:41], v[24:25]
	v_pk_mul_f32 v[74:75], v[42:43], v[26:27]
	v_pk_mul_f32 v[76:77], v[44:45], v[28:29]
	s_waitcnt vmcnt(11) lgkmcnt(3)
	v_mfma_f32_32x32x16_f16 v[34:49], v[46:49], v[122:125], 0
	v_pk_fma_f32 v[66:67], v[2:3], v[50:51], v[66:67]
	v_pk_fma_f32 v[68:69], v[4:5], v[52:53], v[68:69]
	v_pk_fma_f32 v[70:71], v[6:7], v[54:55], v[70:71]
	v_pk_fma_f32 v[72:73], v[8:9], v[56:57], v[72:73]
	v_pk_fma_f32 v[74:75], v[10:11], v[58:59], v[74:75]
	v_pk_fma_f32 v[76:77], v[12:13], v[60:61], v[76:77]
	s_waitcnt lgkmcnt(2)
	v_mfma_f32_32x32x16_f16 v[2:17], v[14:17], v[118:121], 0
	v_pk_mul_f32 v[78:79], v[18:19], v[50:51]
	v_pk_mul_f32 v[80:81], v[20:21], v[52:53]
	v_pk_mul_f32 v[82:83], v[22:23], v[54:55]
	v_pk_mul_f32 v[84:85], v[24:25], v[56:57]
	v_pk_mul_f32 v[86:87], v[26:27], v[58:59]
	v_pk_mul_f32 v[88:89], v[28:29], v[60:61]
	s_waitcnt lgkmcnt(1)
	v_mfma_f32_32x32x16_f16 v[18:33], v[30:33], v[118:121], 0
	s_waitcnt lgkmcnt(0)
	v_mfma_f32_32x32x16_f16 v[50:65], v[62:65], v[122:125], 0
	v_rcp_f32_e32 v78, v78
	v_rcp_f32_e32 v79, v79
	v_rcp_f32_e32 v80, v80
	v_rcp_f32_e32 v81, v81
	v_rcp_f32_e32 v82, v82
	v_rcp_f32_e32 v83, v83
	v_rcp_f32_e32 v84, v84
	v_rcp_f32_e32 v85, v85
	v_rcp_f32_e32 v86, v86
	v_rcp_f32_e32 v87, v87
	v_rcp_f32_e32 v88, v88
	v_rcp_f32_e32 v89, v89
	v_pk_fma_f32 v[90:91], v[66:67], v[78:79], v[90:91]
	v_pk_fma_f32 v[92:93], v[68:69], v[80:81], v[92:93]
	v_pk_fma_f32 v[94:95], v[70:71], v[82:83], v[94:95]
	v_pk_fma_f32 v[96:97], v[72:73], v[84:85], v[96:97]
	v_pk_fma_f32 v[98:99], v[74:75], v[86:87], v[98:99]
	v_pk_fma_f32 v[100:101], v[76:77], v[88:89], v[100:101]
	ds_read_b128 v[46:49], v166 offset:14336
	ds_read_b128 v[14:17], v166 offset:12288
	ds_read_b128 v[30:33], v166 offset:13312
	ds_read_b128 v[62:65], v166 offset:15360
	v_pk_mul_f32 v[66:67], v[34:35], v[18:19]
	v_pk_mul_f32 v[68:69], v[36:37], v[20:21]
	v_pk_mul_f32 v[70:71], v[38:39], v[22:23]
	v_pk_mul_f32 v[72:73], v[40:41], v[24:25]
	v_pk_mul_f32 v[74:75], v[42:43], v[26:27]
	v_pk_mul_f32 v[76:77], v[44:45], v[28:29]
	s_waitcnt vmcnt(9) lgkmcnt(3)
	v_mfma_f32_32x32x16_f16 v[34:49], v[46:49], v[130:133], 0
	v_pk_fma_f32 v[66:67], v[2:3], v[50:51], v[66:67]
	v_pk_fma_f32 v[68:69], v[4:5], v[52:53], v[68:69]
	v_pk_fma_f32 v[70:71], v[6:7], v[54:55], v[70:71]
	v_pk_fma_f32 v[72:73], v[8:9], v[56:57], v[72:73]
	v_pk_fma_f32 v[74:75], v[10:11], v[58:59], v[74:75]
	v_pk_fma_f32 v[76:77], v[12:13], v[60:61], v[76:77]
	s_waitcnt lgkmcnt(2)
	v_mfma_f32_32x32x16_f16 v[2:17], v[14:17], v[126:129], 0
	v_pk_mul_f32 v[78:79], v[18:19], v[50:51]
	v_pk_mul_f32 v[80:81], v[20:21], v[52:53]
	v_pk_mul_f32 v[82:83], v[22:23], v[54:55]
	v_pk_mul_f32 v[84:85], v[24:25], v[56:57]
	v_pk_mul_f32 v[86:87], v[26:27], v[58:59]
	v_pk_mul_f32 v[88:89], v[28:29], v[60:61]
	s_waitcnt lgkmcnt(1)
	v_mfma_f32_32x32x16_f16 v[18:33], v[30:33], v[126:129], 0
	s_waitcnt lgkmcnt(0)
	v_mfma_f32_32x32x16_f16 v[50:65], v[62:65], v[130:133], 0
	v_rcp_f32_e32 v78, v78
	v_rcp_f32_e32 v79, v79
	v_rcp_f32_e32 v80, v80
	v_rcp_f32_e32 v81, v81
	v_rcp_f32_e32 v82, v82
	v_rcp_f32_e32 v83, v83
	v_rcp_f32_e32 v84, v84
	v_rcp_f32_e32 v85, v85
	v_rcp_f32_e32 v86, v86
	v_rcp_f32_e32 v87, v87
	v_rcp_f32_e32 v88, v88
	v_rcp_f32_e32 v89, v89
	v_pk_fma_f32 v[90:91], v[66:67], v[78:79], v[90:91]
	v_pk_fma_f32 v[92:93], v[68:69], v[80:81], v[92:93]
	v_pk_fma_f32 v[94:95], v[70:71], v[82:83], v[94:95]
	v_pk_fma_f32 v[96:97], v[72:73], v[84:85], v[96:97]
	v_pk_fma_f32 v[98:99], v[74:75], v[86:87], v[98:99]
	v_pk_fma_f32 v[100:101], v[76:77], v[88:89], v[100:101]
	ds_read_b128 v[46:49], v166 offset:18432
	ds_read_b128 v[14:17], v166 offset:16384
	ds_read_b128 v[30:33], v166 offset:17408
	ds_read_b128 v[62:65], v166 offset:19456
	v_pk_mul_f32 v[66:67], v[34:35], v[18:19]
	v_pk_mul_f32 v[68:69], v[36:37], v[20:21]
	v_pk_mul_f32 v[70:71], v[38:39], v[22:23]
	v_pk_mul_f32 v[72:73], v[40:41], v[24:25]
	v_pk_mul_f32 v[74:75], v[42:43], v[26:27]
	v_pk_mul_f32 v[76:77], v[44:45], v[28:29]
	s_waitcnt vmcnt(7) lgkmcnt(3)
	v_mfma_f32_32x32x16_f16 v[34:49], v[46:49], v[138:141], 0
	v_pk_fma_f32 v[66:67], v[2:3], v[50:51], v[66:67]
	v_pk_fma_f32 v[68:69], v[4:5], v[52:53], v[68:69]
	v_pk_fma_f32 v[70:71], v[6:7], v[54:55], v[70:71]
	v_pk_fma_f32 v[72:73], v[8:9], v[56:57], v[72:73]
	v_pk_fma_f32 v[74:75], v[10:11], v[58:59], v[74:75]
	v_pk_fma_f32 v[76:77], v[12:13], v[60:61], v[76:77]
	s_waitcnt lgkmcnt(2)
	v_mfma_f32_32x32x16_f16 v[2:17], v[14:17], v[134:137], 0
	v_pk_mul_f32 v[78:79], v[18:19], v[50:51]
	v_pk_mul_f32 v[80:81], v[20:21], v[52:53]
	v_pk_mul_f32 v[82:83], v[22:23], v[54:55]
	v_pk_mul_f32 v[84:85], v[24:25], v[56:57]
	v_pk_mul_f32 v[86:87], v[26:27], v[58:59]
	v_pk_mul_f32 v[88:89], v[28:29], v[60:61]
	s_waitcnt lgkmcnt(1)
	v_mfma_f32_32x32x16_f16 v[18:33], v[30:33], v[134:137], 0
	s_waitcnt lgkmcnt(0)
	v_mfma_f32_32x32x16_f16 v[50:65], v[62:65], v[138:141], 0
	v_rcp_f32_e32 v78, v78
	v_rcp_f32_e32 v79, v79
	v_rcp_f32_e32 v80, v80
	v_rcp_f32_e32 v81, v81
	v_rcp_f32_e32 v82, v82
	v_rcp_f32_e32 v83, v83
	v_rcp_f32_e32 v84, v84
	v_rcp_f32_e32 v85, v85
	v_rcp_f32_e32 v86, v86
	v_rcp_f32_e32 v87, v87
	v_rcp_f32_e32 v88, v88
	v_rcp_f32_e32 v89, v89
	v_pk_fma_f32 v[90:91], v[66:67], v[78:79], v[90:91]
	v_pk_fma_f32 v[92:93], v[68:69], v[80:81], v[92:93]
	v_pk_fma_f32 v[94:95], v[70:71], v[82:83], v[94:95]
	v_pk_fma_f32 v[96:97], v[72:73], v[84:85], v[96:97]
	v_pk_fma_f32 v[98:99], v[74:75], v[86:87], v[98:99]
	v_pk_fma_f32 v[100:101], v[76:77], v[88:89], v[100:101]
	ds_read_b128 v[46:49], v166 offset:22528
	ds_read_b128 v[14:17], v166 offset:20480
	ds_read_b128 v[30:33], v166 offset:21504
	ds_read_b128 v[62:65], v166 offset:23552
	v_pk_mul_f32 v[66:67], v[34:35], v[18:19]
	v_pk_mul_f32 v[68:69], v[36:37], v[20:21]
	v_pk_mul_f32 v[70:71], v[38:39], v[22:23]
	v_pk_mul_f32 v[72:73], v[40:41], v[24:25]
	v_pk_mul_f32 v[74:75], v[42:43], v[26:27]
	v_pk_mul_f32 v[76:77], v[44:45], v[28:29]
	s_waitcnt vmcnt(5) lgkmcnt(3)
	v_mfma_f32_32x32x16_f16 v[34:49], v[46:49], v[146:149], 0
	v_pk_fma_f32 v[66:67], v[2:3], v[50:51], v[66:67]
	v_pk_fma_f32 v[68:69], v[4:5], v[52:53], v[68:69]
	v_pk_fma_f32 v[70:71], v[6:7], v[54:55], v[70:71]
	v_pk_fma_f32 v[72:73], v[8:9], v[56:57], v[72:73]
	v_pk_fma_f32 v[74:75], v[10:11], v[58:59], v[74:75]
	v_pk_fma_f32 v[76:77], v[12:13], v[60:61], v[76:77]
	s_waitcnt lgkmcnt(2)
	v_mfma_f32_32x32x16_f16 v[2:17], v[14:17], v[142:145], 0
	v_pk_mul_f32 v[78:79], v[18:19], v[50:51]
	v_pk_mul_f32 v[80:81], v[20:21], v[52:53]
	v_pk_mul_f32 v[82:83], v[22:23], v[54:55]
	v_pk_mul_f32 v[84:85], v[24:25], v[56:57]
	v_pk_mul_f32 v[86:87], v[26:27], v[58:59]
	v_pk_mul_f32 v[88:89], v[28:29], v[60:61]
	s_waitcnt lgkmcnt(1)
	v_mfma_f32_32x32x16_f16 v[18:33], v[30:33], v[142:145], 0
	s_waitcnt lgkmcnt(0)
	v_mfma_f32_32x32x16_f16 v[50:65], v[62:65], v[146:149], 0
	v_rcp_f32_e32 v78, v78
	v_rcp_f32_e32 v79, v79
	v_rcp_f32_e32 v80, v80
	v_rcp_f32_e32 v81, v81
	v_rcp_f32_e32 v82, v82
	v_rcp_f32_e32 v83, v83
	v_rcp_f32_e32 v84, v84
	v_rcp_f32_e32 v85, v85
	v_rcp_f32_e32 v86, v86
	v_rcp_f32_e32 v87, v87
	v_rcp_f32_e32 v88, v88
	v_rcp_f32_e32 v89, v89
	v_pk_fma_f32 v[90:91], v[66:67], v[78:79], v[90:91]
	v_pk_fma_f32 v[92:93], v[68:69], v[80:81], v[92:93]
	v_pk_fma_f32 v[94:95], v[70:71], v[82:83], v[94:95]
	v_pk_fma_f32 v[96:97], v[72:73], v[84:85], v[96:97]
	v_pk_fma_f32 v[98:99], v[74:75], v[86:87], v[98:99]
	v_pk_fma_f32 v[100:101], v[76:77], v[88:89], v[100:101]
	ds_read_b128 v[46:49], v166 offset:26624
	ds_read_b128 v[14:17], v166 offset:24576
	ds_read_b128 v[30:33], v166 offset:25600
	ds_read_b128 v[62:65], v166 offset:27648
	v_pk_mul_f32 v[66:67], v[34:35], v[18:19]
	v_pk_mul_f32 v[68:69], v[36:37], v[20:21]
	v_pk_mul_f32 v[70:71], v[38:39], v[22:23]
	v_pk_mul_f32 v[72:73], v[40:41], v[24:25]
	v_pk_mul_f32 v[74:75], v[42:43], v[26:27]
	v_pk_mul_f32 v[76:77], v[44:45], v[28:29]
	s_waitcnt vmcnt(3) lgkmcnt(3)
	v_mfma_f32_32x32x16_f16 v[34:49], v[46:49], v[154:157], 0
	v_pk_fma_f32 v[66:67], v[2:3], v[50:51], v[66:67]
	v_pk_fma_f32 v[68:69], v[4:5], v[52:53], v[68:69]
	v_pk_fma_f32 v[70:71], v[6:7], v[54:55], v[70:71]
	v_pk_fma_f32 v[72:73], v[8:9], v[56:57], v[72:73]
	v_pk_fma_f32 v[74:75], v[10:11], v[58:59], v[74:75]
	v_pk_fma_f32 v[76:77], v[12:13], v[60:61], v[76:77]
	s_waitcnt lgkmcnt(2)
	v_mfma_f32_32x32x16_f16 v[2:17], v[14:17], v[150:153], 0
	v_pk_mul_f32 v[78:79], v[18:19], v[50:51]
	v_pk_mul_f32 v[80:81], v[20:21], v[52:53]
	v_pk_mul_f32 v[82:83], v[22:23], v[54:55]
	v_pk_mul_f32 v[84:85], v[24:25], v[56:57]
	v_pk_mul_f32 v[86:87], v[26:27], v[58:59]
	v_pk_mul_f32 v[88:89], v[28:29], v[60:61]
	s_waitcnt lgkmcnt(1)
	v_mfma_f32_32x32x16_f16 v[18:33], v[30:33], v[150:153], 0
	s_waitcnt lgkmcnt(0)
	v_mfma_f32_32x32x16_f16 v[50:65], v[62:65], v[154:157], 0
	v_rcp_f32_e32 v78, v78
	v_rcp_f32_e32 v79, v79
	v_rcp_f32_e32 v80, v80
	v_rcp_f32_e32 v81, v81
	v_rcp_f32_e32 v82, v82
	v_rcp_f32_e32 v83, v83
	v_rcp_f32_e32 v84, v84
	v_rcp_f32_e32 v85, v85
	v_rcp_f32_e32 v86, v86
	v_rcp_f32_e32 v87, v87
	v_rcp_f32_e32 v88, v88
	v_rcp_f32_e32 v89, v89
	v_pk_fma_f32 v[90:91], v[66:67], v[78:79], v[90:91]
	v_pk_fma_f32 v[92:93], v[68:69], v[80:81], v[92:93]
	v_pk_fma_f32 v[94:95], v[70:71], v[82:83], v[94:95]
	v_pk_fma_f32 v[96:97], v[72:73], v[84:85], v[96:97]
	v_pk_fma_f32 v[98:99], v[74:75], v[86:87], v[98:99]
	v_pk_fma_f32 v[100:101], v[76:77], v[88:89], v[100:101]
	ds_read_b128 v[46:49], v166 offset:30720
	ds_read_b128 v[14:17], v166 offset:28672
	ds_read_b128 v[30:33], v166 offset:29696
	ds_read_b128 v[62:65], v166 offset:31744
	v_pk_mul_f32 v[66:67], v[34:35], v[18:19]
	v_pk_mul_f32 v[68:69], v[36:37], v[20:21]
	v_pk_mul_f32 v[70:71], v[38:39], v[22:23]
	v_pk_mul_f32 v[72:73], v[40:41], v[24:25]
	v_pk_mul_f32 v[74:75], v[42:43], v[26:27]
	v_pk_mul_f32 v[76:77], v[44:45], v[28:29]
	s_waitcnt vmcnt(1) lgkmcnt(3)
	v_mfma_f32_32x32x16_f16 v[34:49], v[46:49], v[162:165], 0
	v_pk_fma_f32 v[66:67], v[2:3], v[50:51], v[66:67]
	v_pk_fma_f32 v[68:69], v[4:5], v[52:53], v[68:69]
	v_pk_fma_f32 v[70:71], v[6:7], v[54:55], v[70:71]
	v_pk_fma_f32 v[72:73], v[8:9], v[56:57], v[72:73]
	v_pk_fma_f32 v[74:75], v[10:11], v[58:59], v[74:75]
	v_pk_fma_f32 v[76:77], v[12:13], v[60:61], v[76:77]
	s_waitcnt lgkmcnt(2)
	v_mfma_f32_32x32x16_f16 v[2:17], v[14:17], v[158:161], 0
	v_pk_mul_f32 v[78:79], v[18:19], v[50:51]
	v_pk_mul_f32 v[80:81], v[20:21], v[52:53]
	v_pk_mul_f32 v[82:83], v[22:23], v[54:55]
	v_pk_mul_f32 v[84:85], v[24:25], v[56:57]
	v_pk_mul_f32 v[86:87], v[26:27], v[58:59]
	v_pk_mul_f32 v[88:89], v[28:29], v[60:61]
	s_waitcnt lgkmcnt(1)
	v_mfma_f32_32x32x16_f16 v[18:33], v[30:33], v[158:161], 0
	s_waitcnt lgkmcnt(0)
	v_mfma_f32_32x32x16_f16 v[50:65], v[62:65], v[162:165], 0
	v_rcp_f32_e32 v78, v78
	v_rcp_f32_e32 v79, v79
	v_rcp_f32_e32 v80, v80
	v_rcp_f32_e32 v81, v81
	v_rcp_f32_e32 v82, v82
	v_rcp_f32_e32 v83, v83
	v_rcp_f32_e32 v84, v84
	v_rcp_f32_e32 v85, v85
	v_rcp_f32_e32 v86, v86
	v_rcp_f32_e32 v87, v87
	v_rcp_f32_e32 v88, v88
	v_rcp_f32_e32 v89, v89
	v_pk_fma_f32 v[90:91], v[66:67], v[78:79], v[90:91]
	v_pk_fma_f32 v[92:93], v[68:69], v[80:81], v[92:93]
	v_pk_fma_f32 v[94:95], v[70:71], v[82:83], v[94:95]
	v_pk_fma_f32 v[96:97], v[72:73], v[84:85], v[96:97]
	v_pk_fma_f32 v[98:99], v[74:75], v[86:87], v[98:99]
	v_pk_fma_f32 v[100:101], v[76:77], v[88:89], v[100:101]
	v_pk_mul_f32 v[66:67], v[34:35], v[18:19]
	v_pk_mul_f32 v[68:69], v[36:37], v[20:21]
	v_pk_mul_f32 v[70:71], v[38:39], v[22:23]
	v_pk_mul_f32 v[72:73], v[40:41], v[24:25]
	v_pk_mul_f32 v[74:75], v[42:43], v[26:27]
	v_pk_mul_f32 v[76:77], v[44:45], v[28:29]
	v_pk_fma_f32 v[66:67], v[2:3], v[50:51], v[66:67]
	v_pk_fma_f32 v[68:69], v[4:5], v[52:53], v[68:69]
	v_pk_fma_f32 v[70:71], v[6:7], v[54:55], v[70:71]
	v_pk_fma_f32 v[72:73], v[8:9], v[56:57], v[72:73]
	v_pk_fma_f32 v[74:75], v[10:11], v[58:59], v[74:75]
	v_pk_fma_f32 v[76:77], v[12:13], v[60:61], v[76:77]
	v_pk_mul_f32 v[78:79], v[18:19], v[50:51]
	v_pk_mul_f32 v[80:81], v[20:21], v[52:53]
	v_pk_mul_f32 v[82:83], v[22:23], v[54:55]
	v_pk_mul_f32 v[84:85], v[24:25], v[56:57]
	v_pk_mul_f32 v[86:87], v[26:27], v[58:59]
	v_pk_mul_f32 v[88:89], v[28:29], v[60:61]
	v_rcp_f32_e32 v78, v78
	v_rcp_f32_e32 v79, v79
	v_rcp_f32_e32 v80, v80
	v_rcp_f32_e32 v81, v81
	v_rcp_f32_e32 v82, v82
	v_rcp_f32_e32 v83, v83
	v_rcp_f32_e32 v84, v84
	v_rcp_f32_e32 v85, v85
	v_rcp_f32_e32 v86, v86
	v_rcp_f32_e32 v87, v87
	v_rcp_f32_e32 v88, v88
	v_rcp_f32_e32 v89, v89
	v_pk_fma_f32 v[90:91], v[66:67], v[78:79], v[90:91]
	v_pk_fma_f32 v[92:93], v[68:69], v[80:81], v[92:93]
	v_pk_fma_f32 v[94:95], v[70:71], v[82:83], v[94:95]
	v_pk_fma_f32 v[96:97], v[72:73], v[84:85], v[96:97]
	v_pk_fma_f32 v[98:99], v[74:75], v[86:87], v[98:99]
	v_pk_fma_f32 v[100:101], v[76:77], v[88:89], v[100:101]
	v_fma_f32 v66, v90, -2.0, s28
	v_subrev_f32_e32 v66, s29, v66
	v_mul_f32_e32 v66, 0x3fb8aa3b, v66
	v_exp_f32_e32 v66, v66
	v_fma_f32 v67, v91, -2.0, s28
	v_subrev_f32_e32 v67, s29, v67
	v_mul_f32_e32 v67, 0x3fb8aa3b, v67
	v_exp_f32_e32 v67, v67
	v_fma_f32 v68, v92, -2.0, s28
	v_subrev_f32_e32 v68, s29, v68
	v_mul_f32_e32 v68, 0x3fb8aa3b, v68
	v_exp_f32_e32 v68, v68
	v_fma_f32 v69, v93, -2.0, s28
	v_subrev_f32_e32 v69, s29, v69
	v_mul_f32_e32 v69, 0x3fb8aa3b, v69
	v_exp_f32_e32 v69, v69
	v_fma_f32 v70, v94, -2.0, s28
	v_subrev_f32_e32 v70, s29, v70
	v_mul_f32_e32 v70, 0x3fb8aa3b, v70
	v_exp_f32_e32 v70, v70
	v_fma_f32 v71, v95, -2.0, s28
	v_subrev_f32_e32 v71, s29, v71
	v_mul_f32_e32 v71, 0x3fb8aa3b, v71
	v_exp_f32_e32 v71, v71
	v_fma_f32 v72, v96, -2.0, s28
	v_subrev_f32_e32 v72, s29, v72
	v_mul_f32_e32 v72, 0x3fb8aa3b, v72
	v_exp_f32_e32 v72, v72
	v_fma_f32 v73, v97, -2.0, s28
	v_subrev_f32_e32 v73, s29, v73
	v_mul_f32_e32 v73, 0x3fb8aa3b, v73
	v_exp_f32_e32 v73, v73
	v_fma_f32 v74, v98, -2.0, s28
	v_subrev_f32_e32 v74, s29, v74
	v_mul_f32_e32 v74, 0x3fb8aa3b, v74
	v_exp_f32_e32 v74, v74
	v_fma_f32 v75, v99, -2.0, s28
	v_subrev_f32_e32 v75, s29, v75
	v_mul_f32_e32 v75, 0x3fb8aa3b, v75
	v_exp_f32_e32 v75, v75
	v_fma_f32 v76, v100, -2.0, s28
	v_subrev_f32_e32 v76, s29, v76
	v_mul_f32_e32 v76, 0x3fb8aa3b, v76
	v_exp_f32_e32 v76, v76
	v_fma_f32 v77, v101, -2.0, s28
	v_subrev_f32_e32 v77, s29, v77
	v_mul_f32_e32 v77, 0x3fb8aa3b, v77
	v_exp_f32_e32 v77, v77
	s_nop 0
	v_cvt_f16_f32_e32 v66, v66
	v_cvt_f16_f32_e32 v67, v67
	v_cvt_f16_f32_e32 v68, v68
	v_cvt_f16_f32_e32 v69, v69
	v_cvt_f16_f32_e32 v70, v70
	v_cvt_f16_f32_e32 v71, v71
	v_cvt_f16_f32_e32 v72, v72
	v_cvt_f16_f32_e32 v73, v73
	v_cvt_f16_f32_e32 v74, v74
	v_cvt_f16_f32_e32 v75, v75
	v_cvt_f16_f32_e32 v76, v76
	v_cvt_f16_f32_e32 v77, v77
	ds_write_b16 v1, v66
	ds_write_b16 v1, v67 offset:800
	ds_write_b16 v1, v68 offset:1600
	ds_write_b16 v1, v69 offset:2400
	ds_write_b16 v1, v70 offset:6400
	ds_write_b16 v1, v71 offset:7200
	ds_write_b16 v1, v72 offset:8000
	ds_write_b16 v1, v73 offset:8800
	ds_write_b16 v1, v74 offset:12800
	ds_write_b16 v1, v75 offset:13600
	ds_write_b16 v1, v76 offset:14400
	ds_write_b16 v1, v77 offset:15200
	s_cmpk_gt_u32 s49, 0xff
	s_cbranch_scc1 .Lf_wo_done
	s_waitcnt vmcnt(0)
	v_cvt_f16_f32_e32 v2, v102
	v_cvt_f16_f32_e32 v5, v105
	v_cvt_pk_f16_f32 v3, v103, v104
	v_pack_b32_f16 v2, v2, v3
	v_alignbit_b32 v3, v5, v3, 16
	v_and_b32_e32 v6, 0xff, v0
	v_lshlrev_b32_e32 v6, 3, v6
	s_lshl_b32 s22, s42, 1
	v_add_u32_e32 v6, s22, v6
	global_store_dwordx2 v6, v[2:3], s[18:19]
